# output P32 gather/store phase moved from k_main into k_t2 (after tier-2 items; tier-2 tokens marked -1 and skipped) to overlap tier-2 latency with the store stream
# baseline (speedup 1.0000x reference)
.LBB1_45:
	s_or_b64 exec, exec, s[0:1]
	v_fma_f32 v12, s25, v28, v27
	v_sub_f32_e32 v11, v11, v13
	v_cmp_nlt_f32_e32 vcc, v11, v12
	s_and_saveexec_b64 s[0:1], vcc
	s_xor_b64 s[0:1], exec, s[0:1]
	v_cmp_eq_u32_e32 vcc, s24, v129
	s_nop 1
	v_cndmask_b32_e32 v22, v22, v15, vcc
	s_andn2_saveexec_b64 s[0:1], s[0:1]
	s_cbranch_execz .LBB1_14
	v_cmp_eq_u32_e32 vcc, s24, v129
	s_nop 1
	v_cndmask_b32_e64 v22, v22, -1, vcc
	s_and_saveexec_b64 s[22:23], s[10:11]
	s_cbranch_execz .LBB1_13
	s_mov_b64 s[26:27], exec
	v_mbcnt_lo_u32_b32 v11, s26, 0
	v_mbcnt_hi_u32_b32 v11, s27, v11
	v_cmp_eq_u32_e32 vcc, 0, v11
	s_and_saveexec_b64 s[24:25], vcc
	s_cbranch_execz .LBB1_12
	s_bcnt1_i32_b64 s13, s[26:27]
	v_mov_b32_e32 v12, s13
	global_atomic_add v12, v131, v12, s[18:19] sc0
	s_branch .LBB1_12

.LBB1_53:
	s_or_b64 exec, exec, s[0:1]
	s_nop 4
	v_add_f32_dpp v2, v123, v123 quad_perm:[1,0,3,2] row_mask:0xf bank_mask:0xf bound_ctrl:1
	s_nop 1
	v_add_f32_dpp v2, v2, v2 quad_perm:[2,3,0,1] row_mask:0xf bank_mask:0xf bound_ctrl:1
	v_mov_b32_e32 v3, v2
	s_nop 1
	v_mov_b32_dpp v3, v3 row_shl:4 row_mask:0xf bank_mask:0x5
	s_nop 1
	v_mov_b32_dpp v3, v2 row_shr:4 row_mask:0xf bank_mask:0xa
	v_add_f32_e32 v2, v2, v3
	s_nop 1
	v_add_f32_dpp v2, v2, v2 row_ror:8 row_mask:0xf bank_mask:0xf bound_ctrl:1
	v_mov_b32_e32 v3, v2
	s_nop 1
	v_permlane16_swap_b32_e32 v2, v3
	v_add_f32_e32 v2, v2, v3
	v_mov_b32_e32 v3, v2
	s_nop 1
	v_permlane32_swap_b32_e32 v2, v3
	s_and_saveexec_b64 s[0:1], s[10:11]
	v_mov_b32_e32 v4, 0x18040
	v_lshl_or_b32 v1, v1, 2, v4
	v_add_f32_e32 v2, v2, v3
	ds_write_b32 v1, v2
	s_or_b64 exec, exec, s[0:1]
	s_mov_b32 s3, 0
	v_cmp_eq_u32_e32 vcc, 0, v0
	s_waitcnt lgkmcnt(0)
	s_barrier
	s_and_saveexec_b64 s[0:1], vcc
	s_cbranch_execz .LBB1_59
	v_mov_b32_e32 v4, 0x18050
	v_mov_b32_e32 v0, 0x18040
	ds_read_b128 v[0:3], v0
	ds_read_b128 v[4:7], v4
	s_lshl_b64 s[0:1], s[2:3], 2
	s_add_u32 s0, s30, s0
	s_addc_u32 s1, s31, s1
	s_waitcnt lgkmcnt(1)
	v_mov_b32_e32 v8, v0
	s_waitcnt lgkmcnt(0)
	v_mov_b32_e32 v9, v4
	v_mov_b32_e32 v4, v1
	v_pk_add_f32 v[0:1], v[8:9], v[4:5]
	v_mov_b32_e32 v4, v2
	v_mov_b32_e32 v5, v6
	v_mov_b32_e32 v6, v3
	v_pk_add_f32 v[2:3], v[4:5], v[6:7]
	s_nop 0
	v_pk_add_f32 v[0:1], v[0:1], v[2:3]
	s_nop 0
	v_add_f32_e32 v0, v0, v1
	v_mov_b32_e32 v1, 0
	global_store_dword v1, v0, s[0:1]

_Z4k_t2PKfS0_S0_S0_S0_S0_PK15HIP_vector_typeIiLj4EEPKiPdPiS0_S0_Pf:
	s_mov_b32 s100, s0
	s_mov_b32 s101, s1
	v_mov_b32_e32 v159, v0
	s_load_dword s33, s[0:1], 0x68
	s_load_dwordx2 s[34:35], s[0:1], 0x60
	s_load_dwordx2 s[4:5], s[0:1], 0x38
	s_load_dwordx8 s[16:23], s[0:1], 0x0
	s_load_dwordx4 s[24:27], s[0:1], 0x40
	s_load_dwordx2 s[90:91], s[0:1], 0x30
	v_and_b32_e32 v66, 63, v0
	v_lshrrev_b32_e32 v1, 6, v0
	s_waitcnt lgkmcnt(0)
	s_add_i32 s3, s33, -1
	s_cmp_lg_u32 s2, s3
	v_lshlrev_b32_e32 v2, 2, v0
	v_cmp_eq_u32_e32 vcc, 0, v66
	s_cbranch_scc1 .LBB2_6
	s_load_dwordx2 s[6:7], s[0:1], 0x58
	s_waitcnt lgkmcnt(0)
	global_load_dword v3, v2, s[6:7]
	s_waitcnt vmcnt(0)
	s_nop 0
	v_add_f32_dpp v3, v3, v3 quad_perm:[1,0,3,2] row_mask:0xf bank_mask:0xf bound_ctrl:1
	s_nop 1
	v_add_f32_dpp v3, v3, v3 quad_perm:[2,3,0,1] row_mask:0xf bank_mask:0xf bound_ctrl:1
	v_mov_b32_e32 v4, v3
	s_nop 1
	v_mov_b32_dpp v4, v4 row_shl:4 row_mask:0xf bank_mask:0x5
	s_nop 1
	v_mov_b32_dpp v4, v3 row_shr:4 row_mask:0xf bank_mask:0xa
	v_add_f32_e32 v3, v3, v4
	s_nop 1
	v_add_f32_dpp v3, v3, v3 row_ror:8 row_mask:0xf bank_mask:0xf bound_ctrl:1
	v_mov_b32_e32 v4, v3
	s_nop 1
	v_permlane16_swap_b32_e32 v3, v4
	v_add_f32_e32 v3, v3, v4
	v_mov_b32_e32 v4, v3
	s_nop 1
	v_permlane32_swap_b32_e32 v3, v4
	s_and_saveexec_b64 s[6:7], vcc
	v_lshlrev_b32_e32 v5, 2, v1
	v_add_f32_e32 v3, v3, v4
	ds_write_b32 v5, v3 offset:4096
	s_or_b64 exec, exec, s[6:7]
	v_cmp_eq_u32_e32 vcc, 0, v0
	s_waitcnt lgkmcnt(0)
	s_barrier
	s_and_saveexec_b64 s[6:7], vcc
	s_cbranch_execz .LBB2_5
	v_mov_b32_e32 v3, 0
	v_mov_b32_e32 v6, 0x1004
	ds_read_b64 v[4:5], v3 offset:4096
	ds_read2_b32 v[6:7], v6 offset1:1
	s_waitcnt lgkmcnt(1)
	ds_read_b32 v5, v3 offset:4108
	s_waitcnt lgkmcnt(0)
	v_pk_add_f32 v[4:5], v[6:7], v[4:5]
	s_nop 0
	v_add_f32_e32 v3, v4, v5
	v_mul_f32_e32 v3, 0x32a00000, v3
	v_mov_b32_e32 v4, 0x4040000
	global_store_dword v4, v3, s[34:35]

.LBB2_43:
	s_mov_b64 exec, -1
	s_load_dwordx2 s[14:15], s[100:101], 0x60
	s_load_dwordx2 s[38:39], s[100:101], 0x50
	s_and_b32 s2, s2, 0xff
	v_and_b32_e32 v100, 63, v159
	v_lshrrev_b32_e32 v101, 6, v159
	s_lshl_b32 s3, s2, 8
	v_lshl_or_b32 v102, v101, 6, s3
	v_add_u32_e32 v103, v102, v100
	v_lshlrev_b32_e32 v103, 2, v103
	v_lshlrev_b32_e32 v124, 4, v100
	v_mov_b32_e32 v125, 0
	v_lshlrev_b32_e32 v126, 10, v102
	v_mov_b32_e32 v127, 0
	s_waitcnt lgkmcnt(0)
	s_add_u32 s8, s14, 0x4000000
	s_addc_u32 s9, s15, 0
	global_load_dword v22, v103, s[8:9]
	v_lshl_add_u64 v[4:5], v[126:127], 0, v[124:125]
	v_lshl_add_u64 v[4:5], s[14:15], 0, v[4:5]
	s_mov_b64 s[0:1], 0x3c00
	v_lshl_add_u64 v[2:3], s[38:39], 0, v[124:125]
	v_lshl_add_u64 v[4:5], v[4:5], 0, s[0:1]
	s_waitcnt vmcnt(0)
	v_cvt_i32_f32_e32 v22, v22
	s_nop 0
	v_cmp_gt_i32_e64 s[44:45], 0, v22
	v_max_i32_e32 v22, 0, v22
	s_mov_b32 s3, 0
	s_movk_i32 s6, 0xe000
	s_movk_i32 s7, 0xf000
	s_mov_b64 s[4:5], 0x4000
	s_nop 3
.Lmy_sloop:
	v_readlane_b32 s0, v22, s3
	s_add_i32 s8, s3, 1
	s_add_i32 s9, s3, 2
	s_add_i32 s13, s3, 3
	s_add_i32 s15, s3, 4
	s_add_i32 s17, s3, 5
	s_add_i32 s19, s3, 6
	s_add_i32 s21, s3, 7
	s_add_i32 s23, s3, 8
	s_add_i32 s25, s3, 9
	s_add_i32 s27, s3, 10
	s_add_i32 s29, s3, 11
	s_add_i32 s33, s3, 12
	s_add_i32 s35, s3, 13
	s_add_i32 s37, s3, 14
	s_add_i32 s39, s3, 15
	s_ashr_i32 s1, s0, 31
	v_readlane_b32 s8, v22, s8
	v_readlane_b32 s12, v22, s9
	v_readlane_b32 s14, v22, s13
	v_readlane_b32 s16, v22, s15
	v_readlane_b32 s18, v22, s17
	v_readlane_b32 s20, v22, s19
	v_readlane_b32 s22, v22, s21
	v_readlane_b32 s24, v22, s23
	v_readlane_b32 s26, v22, s25
	v_readlane_b32 s28, v22, s27
	v_readlane_b32 s34, v22, s29
	v_readlane_b32 s36, v22, s33
	v_readlane_b32 s38, v22, s35
	v_readlane_b32 s40, v22, s37
	v_readlane_b32 s42, v22, s39
	s_lshl_b64 s[0:1], s[0:1], 10
	s_ashr_i32 s9, s8, 31
	s_ashr_i32 s13, s12, 31
	s_ashr_i32 s15, s14, 31
	s_ashr_i32 s17, s16, 31
	s_ashr_i32 s19, s18, 31
	s_ashr_i32 s21, s20, 31
	s_ashr_i32 s23, s22, 31
	s_ashr_i32 s25, s24, 31
	s_ashr_i32 s27, s26, 31
	s_ashr_i32 s29, s28, 31
	s_ashr_i32 s35, s34, 31
	s_ashr_i32 s37, s36, 31
	s_ashr_i32 s39, s38, 31
	s_ashr_i32 s41, s40, 31
	s_ashr_i32 s43, s42, 31
	v_lshl_add_u64 v[68:69], v[2:3], 0, s[0:1]
	s_lshl_b64 s[0:1], s[8:9], 10
	s_lshl_b64 s[8:9], s[12:13], 10
	s_lshl_b64 s[12:13], s[14:15], 10
	s_lshl_b64 s[14:15], s[16:17], 10
	s_lshl_b64 s[16:17], s[18:19], 10
	s_lshl_b64 s[18:19], s[20:21], 10
	s_lshl_b64 s[20:21], s[22:23], 10
	s_lshl_b64 s[22:23], s[24:25], 10
	s_lshl_b64 s[24:25], s[26:27], 10
	s_lshl_b64 s[26:27], s[28:29], 10
	s_lshl_b64 s[28:29], s[34:35], 10
	s_lshl_b64 s[34:35], s[36:37], 10
	s_lshl_b64 s[36:37], s[38:39], 10
	s_lshl_b64 s[38:39], s[40:41], 10
	s_lshl_b64 s[40:41], s[42:43], 10
	v_lshl_add_u64 v[70:71], v[2:3], 0, s[0:1]
	v_lshl_add_u64 v[72:73], v[2:3], 0, s[8:9]
	v_lshl_add_u64 v[74:75], v[2:3], 0, s[12:13]
	v_lshl_add_u64 v[76:77], v[2:3], 0, s[14:15]
	v_lshl_add_u64 v[78:79], v[2:3], 0, s[16:17]
	v_lshl_add_u64 v[80:81], v[2:3], 0, s[18:19]
	v_lshl_add_u64 v[82:83], v[2:3], 0, s[20:21]
	v_lshl_add_u64 v[84:85], v[2:3], 0, s[22:23]
	v_lshl_add_u64 v[86:87], v[2:3], 0, s[24:25]
	v_lshl_add_u64 v[88:89], v[2:3], 0, s[26:27]
	v_lshl_add_u64 v[90:91], v[2:3], 0, s[28:29]
	v_lshl_add_u64 v[92:93], v[2:3], 0, s[34:35]
	v_lshl_add_u64 v[94:95], v[2:3], 0, s[36:37]
	v_lshl_add_u64 v[96:97], v[2:3], 0, s[38:39]
	v_lshl_add_u64 v[98:99], v[2:3], 0, s[40:41]
	global_load_dwordx4 v[6:9], v[68:69], off
	global_load_dwordx4 v[10:13], v[70:71], off
	global_load_dwordx4 v[14:17], v[72:73], off
	global_load_dwordx4 v[18:21], v[74:75], off
	global_load_dwordx4 v[24:27], v[76:77], off
	global_load_dwordx4 v[28:31], v[78:79], off
	global_load_dwordx4 v[32:35], v[80:81], off
	global_load_dwordx4 v[36:39], v[82:83], off
	global_load_dwordx4 v[40:43], v[84:85], off
	global_load_dwordx4 v[44:47], v[86:87], off
	global_load_dwordx4 v[48:51], v[88:89], off
	global_load_dwordx4 v[52:55], v[90:91], off
	global_load_dwordx4 v[56:59], v[92:93], off
	global_load_dwordx4 v[60:63], v[94:95], off
	global_load_dwordx4 v[64:67], v[96:97], off
	global_load_dwordx4 v[68:71], v[98:99], off
	v_add_co_u32_e64 v74, s[0:1], s6, v4
	v_add_co_u32_e32 v72, vcc, 0xffffd000, v4
	s_nop 0
	v_addc_co_u32_e64 v75, s[0:1], -1, v5, s[0:1]
	v_add_co_u32_e64 v76, s[0:1], s7, v4
	s_add_i32 s3, s3, 16
	v_addc_co_u32_e32 v73, vcc, -1, v5, vcc
	v_addc_co_u32_e64 v77, s[0:1], -1, v5, s[0:1]
	s_waitcnt vmcnt(0)
	s_add_i32 s46, s3, -16
	s_bitcmp1_b64 s[44:45], s46
	s_cbranch_scc1 .Lmy_sk0
	global_store_dwordx4 v[72:73], v[6:9], off offset:-3072 nt
.Lmy_sk0:
	s_add_i32 s46, s3, -15
	s_bitcmp1_b64 s[44:45], s46
	s_cbranch_scc1 .Lmy_sk1
	global_store_dwordx4 v[72:73], v[10:13], off offset:-2048 nt
.Lmy_sk1:
	s_add_i32 s46, s3, -14
	s_bitcmp1_b64 s[44:45], s46
	s_cbranch_scc1 .Lmy_sk2
	global_store_dwordx4 v[72:73], v[14:17], off offset:-1024 nt
.Lmy_sk2:
	s_add_i32 s46, s3, -13
	s_bitcmp1_b64 s[44:45], s46
	s_cbranch_scc1 .Lmy_sk3
	global_store_dwordx4 v[72:73], v[18:21], off nt
.Lmy_sk3:
	s_add_i32 s46, s3, -12
	s_bitcmp1_b64 s[44:45], s46
	s_cbranch_scc1 .Lmy_sk4
	global_store_dwordx4 v[74:75], v[24:27], off offset:-3072 nt
.Lmy_sk4:
	s_add_i32 s46, s3, -11
	s_bitcmp1_b64 s[44:45], s46
	s_cbranch_scc1 .Lmy_sk5
	global_store_dwordx4 v[74:75], v[28:31], off offset:-2048 nt
.Lmy_sk5:
	s_add_i32 s46, s3, -10
	s_bitcmp1_b64 s[44:45], s46
	s_cbranch_scc1 .Lmy_sk6
	global_store_dwordx4 v[74:75], v[32:35], off offset:-1024 nt
.Lmy_sk6:
	s_add_i32 s46, s3, -9
	s_bitcmp1_b64 s[44:45], s46
	s_cbranch_scc1 .Lmy_sk7
	global_store_dwordx4 v[74:75], v[36:39], off nt
.Lmy_sk7:
	s_add_i32 s46, s3, -8
	s_bitcmp1_b64 s[44:45], s46
	s_cbranch_scc1 .Lmy_sk8
	global_store_dwordx4 v[76:77], v[40:43], off offset:-3072 nt
.Lmy_sk8:
	s_add_i32 s46, s3, -7
	s_bitcmp1_b64 s[44:45], s46
	s_cbranch_scc1 .Lmy_sk9
	global_store_dwordx4 v[76:77], v[44:47], off offset:-2048 nt
.Lmy_sk9:
	s_add_i32 s46, s3, -6
	s_bitcmp1_b64 s[44:45], s46
	s_cbranch_scc1 .Lmy_sk10
	global_store_dwordx4 v[76:77], v[48:51], off offset:-1024 nt
.Lmy_sk10:
	s_add_i32 s46, s3, -5
	s_bitcmp1_b64 s[44:45], s46
	s_cbranch_scc1 .Lmy_sk11
	global_store_dwordx4 v[4:5], v[52:55], off offset:-4096 nt
.Lmy_sk11:
	s_add_i32 s46, s3, -4
	s_bitcmp1_b64 s[44:45], s46
	s_cbranch_scc1 .Lmy_sk12
	global_store_dwordx4 v[4:5], v[56:59], off offset:-3072 nt
.Lmy_sk12:
	s_add_i32 s46, s3, -3
	s_bitcmp1_b64 s[44:45], s46
	s_cbranch_scc1 .Lmy_sk13
	global_store_dwordx4 v[4:5], v[60:63], off offset:-2048 nt
.Lmy_sk13:
	s_add_i32 s46, s3, -2
	s_bitcmp1_b64 s[44:45], s46
	s_cbranch_scc1 .Lmy_sk14
	global_store_dwordx4 v[4:5], v[64:67], off offset:-1024 nt
.Lmy_sk14:
	s_add_i32 s46, s3, -1
	s_bitcmp1_b64 s[44:45], s46
	s_cbranch_scc1 .Lmy_sk15
	global_store_dwordx4 v[4:5], v[68:71], off nt
.Lmy_sk15:
	v_lshl_add_u64 v[4:5], v[4:5], 0, s[4:5]
	s_cmp_eq_u32 s3, 64
	s_cbranch_scc0 .Lmy_sloop
	s_endpgm

	.amdhsa_kernel _Z4k_t2PKfS0_S0_S0_S0_S0_PK15HIP_vector_typeIiLj4EEPKiPdPiS0_S0_Pf
		.amdhsa_group_segment_fixed_size 4120
		.amdhsa_private_segment_fixed_size 0
		.amdhsa_kernarg_size 360
		.amdhsa_user_sgpr_count 2
		.amdhsa_user_sgpr_dispatch_ptr 0
		.amdhsa_user_sgpr_queue_ptr 0
		.amdhsa_user_sgpr_kernarg_segment_ptr 1
		.amdhsa_user_sgpr_dispatch_id 0
		.amdhsa_user_sgpr_kernarg_preload_length 0
		.amdhsa_user_sgpr_kernarg_preload_offset 0
		.amdhsa_user_sgpr_private_segment_size 0
		.amdhsa_uses_dynamic_stack 0
		.amdhsa_enable_private_segment 0
		.amdhsa_system_sgpr_workgroup_id_x 1
		.amdhsa_system_sgpr_workgroup_id_y 0
		.amdhsa_system_sgpr_workgroup_id_z 0
		.amdhsa_system_sgpr_workgroup_info 0
		.amdhsa_system_vgpr_workitem_id 0
		.amdhsa_next_free_vgpr 160
		.amdhsa_next_free_sgpr 102
		.amdhsa_accum_offset 160
		.amdhsa_reserve_vcc 1
		.amdhsa_float_round_mode_32 0
		.amdhsa_float_round_mode_16_64 0
		.amdhsa_float_denorm_mode_32 3
		.amdhsa_float_denorm_mode_16_64 3
		.amdhsa_dx10_clamp 1
		.amdhsa_ieee_mode 1
		.amdhsa_fp16_overflow 0
		.amdhsa_tg_split 0
		.amdhsa_exception_fp_ieee_invalid_op 0
		.amdhsa_exception_fp_denorm_src 0
		.amdhsa_exception_fp_ieee_div_zero 0
		.amdhsa_exception_fp_ieee_overflow 0
		.amdhsa_exception_fp_ieee_underflow 0
		.amdhsa_exception_fp_ieee_inexact 0
		.amdhsa_exception_int_div_zero 0
	.end_amdhsa_kernel

amdhsa.kernels:
  - .agpr_count:     0
    .args:
      - .actual_access:  read_only
        .address_space:  global
        .offset:         0
        .size:           8
        .value_kind:     global_buffer
      - .actual_access:  read_only
        .address_space:  global
        .offset:         8
        .size:           8
        .value_kind:     global_buffer
      - .actual_access:  read_only
        .address_space:  global
        .offset:         16
        .size:           8
        .value_kind:     global_buffer
      - .actual_access:  read_only
        .address_space:  global
        .offset:         24
        .size:           8
        .value_kind:     global_buffer
      - .actual_access:  read_only
        .address_space:  global
        .offset:         32
        .size:           8
        .value_kind:     global_buffer
      - .actual_access:  write_only
        .address_space:  global
        .offset:         40
        .size:           8
        .value_kind:     global_buffer
      - .actual_access:  write_only
        .address_space:  global
        .offset:         48
        .size:           8
        .value_kind:     global_buffer
      - .actual_access:  write_only
        .address_space:  global
        .offset:         56
        .size:           8
        .value_kind:     global_buffer
      - .actual_access:  write_only
        .address_space:  global
        .offset:         64
        .size:           8
        .value_kind:     global_buffer
      - .actual_access:  write_only
        .address_space:  global
        .offset:         72
        .size:           8
        .value_kind:     global_buffer
      - .actual_access:  write_only
        .address_space:  global
        .offset:         80
        .size:           8
        .value_kind:     global_buffer
      - .actual_access:  write_only
        .address_space:  global
        .offset:         88
        .size:           8
        .value_kind:     global_buffer
      - .actual_access:  write_only
        .address_space:  global
        .offset:         96
        .size:           8
        .value_kind:     global_buffer
    .group_segment_fixed_size: 73760
    .kernarg_segment_align: 8
    .kernarg_segment_size: 104
    .language:       OpenCL C
    .language_version:
      - 2
      - 0
    .max_flat_workgroup_size: 512
    .name:           _Z6k_prepPKfS0_S0_S0_S0_PfPDF16_S1_S1_S1_S1_S1_Pi
    .private_segment_fixed_size: 0
    .sgpr_count:     35
    .sgpr_spill_count: 0
    .symbol:         _Z6k_prepPKfS0_S0_S0_S0_PfPDF16_S1_S1_S1_S1_S1_Pi.kd
    .uniform_work_group_size: 1
    .uses_dynamic_stack: false
    .vgpr_count:     127
    .vgpr_spill_count: 0
    .wavefront_size: 64
  - .agpr_count:     0
    .args:
      - .actual_access:  read_only
        .address_space:  global
        .offset:         0
        .size:           8
        .value_kind:     global_buffer
      - .actual_access:  read_only
        .address_space:  global
        .offset:         8
        .size:           8
        .value_kind:     global_buffer
      - .actual_access:  read_only
        .address_space:  global
        .offset:         16
        .size:           8
        .value_kind:     global_buffer
      - .address_space:  global
        .offset:         24
        .size:           8
        .value_kind:     global_buffer
      - .actual_access:  read_only
        .address_space:  global
        .offset:         32
        .size:           8
        .value_kind:     global_buffer
      - .actual_access:  read_only
        .address_space:  global
        .offset:         40
        .size:           8
        .value_kind:     global_buffer
      - .actual_access:  read_only
        .address_space:  global
        .offset:         48
        .size:           8
        .value_kind:     global_buffer
      - .actual_access:  read_only
        .address_space:  global
        .offset:         56
        .size:           8
        .value_kind:     global_buffer
      - .actual_access:  read_only
        .address_space:  global
        .offset:         64
        .size:           8
        .value_kind:     global_buffer
      - .actual_access:  read_only
        .address_space:  global
        .offset:         72
        .size:           8
        .value_kind:     global_buffer
      - .actual_access:  write_only
        .address_space:  global
        .offset:         80
        .size:           8
        .value_kind:     global_buffer
      - .actual_access:  write_only
        .address_space:  global
        .offset:         88
        .size:           8
        .value_kind:     global_buffer
      - .address_space:  global
        .offset:         96
        .size:           8
        .value_kind:     global_buffer
      - .actual_access:  write_only
        .address_space:  global
        .offset:         104
        .size:           8
        .value_kind:     global_buffer
    .group_segment_fixed_size: 105056
    .kernarg_segment_align: 8
    .kernarg_segment_size: 112
    .language:       OpenCL C
    .language_version:
      - 2
      - 0
    .max_flat_workgroup_size: 512
    .name:           _Z6k_mainPKfS0_S0_PKDF16_S0_S0_S0_S0_S0_S0_PfP15HIP_vector_typeIiLj4EEPiS3_
    .private_segment_fixed_size: 0
    .sgpr_count:     105
    .sgpr_spill_count: 0
    .symbol:         _Z6k_mainPKfS0_S0_PKDF16_S0_S0_S0_S0_S0_S0_PfP15HIP_vector_typeIiLj4EEPiS3_.kd
    .uniform_work_group_size: 1
    .uses_dynamic_stack: false
    .vgpr_count:     248
    .vgpr_spill_count: 0
    .wavefront_size: 64
  - .agpr_count:     0
    .args:
      - .actual_access:  read_only
        .address_space:  global
        .offset:         0
        .size:           8
        .value_kind:     global_buffer
      - .actual_access:  read_only
        .address_space:  global
        .offset:         8
        .size:           8
        .value_kind:     global_buffer
      - .actual_access:  read_only
        .address_space:  global
        .offset:         16
        .size:           8
        .value_kind:     global_buffer
      - .actual_access:  read_only
        .address_space:  global
        .offset:         24
        .size:           8
        .value_kind:     global_buffer
      - .actual_access:  read_only
        .address_space:  global
        .offset:         32
        .size:           8
        .value_kind:     global_buffer
      - .actual_access:  read_only
        .address_space:  global
        .offset:         40
        .size:           8
        .value_kind:     global_buffer
      - .actual_access:  read_only
        .address_space:  global
        .offset:         48
        .size:           8
        .value_kind:     global_buffer
      - .actual_access:  read_only
        .address_space:  global
        .offset:         56
        .size:           8
        .value_kind:     global_buffer
      - .address_space:  global
        .offset:         64
        .size:           8
        .value_kind:     global_buffer
      - .address_space:  global
        .offset:         72
        .size:           8
        .value_kind:     global_buffer
      - .actual_access:  read_only
        .address_space:  global
        .offset:         80
        .size:           8
        .value_kind:     global_buffer
      - .actual_access:  read_only
        .address_space:  global
        .offset:         88
        .size:           8
        .value_kind:     global_buffer
      - .actual_access:  write_only
        .address_space:  global
        .offset:         96
        .size:           8
        .value_kind:     global_buffer
      - .offset:         104
        .size:           4
        .value_kind:     hidden_block_count_x
      - .offset:         108
        .size:           4
        .value_kind:     hidden_block_count_y
      - .offset:         112
        .size:           4
        .value_kind:     hidden_block_count_z
      - .offset:         116
        .size:           2
        .value_kind:     hidden_group_size_x
      - .offset:         118
        .size:           2
        .value_kind:     hidden_group_size_y
      - .offset:         120
        .size:           2
        .value_kind:     hidden_group_size_z
      - .offset:         122
        .size:           2
        .value_kind:     hidden_remainder_x
      - .offset:         124
        .size:           2
        .value_kind:     hidden_remainder_y
      - .offset:         126
        .size:           2
        .value_kind:     hidden_remainder_z
      - .offset:         144
        .size:           8
        .value_kind:     hidden_global_offset_x
      - .offset:         152
        .size:           8
        .value_kind:     hidden_global_offset_y
      - .offset:         160
        .size:           8
        .value_kind:     hidden_global_offset_z
      - .offset:         168
        .size:           2
        .value_kind:     hidden_grid_dims
    .group_segment_fixed_size: 4120
    .kernarg_segment_align: 8
    .kernarg_segment_size: 360
    .language:       OpenCL C
    .language_version:
      - 2
      - 0
    .max_flat_workgroup_size: 256
    .name:           _Z4k_t2PKfS0_S0_S0_S0_S0_PK15HIP_vector_typeIiLj4EEPKiPdPiS0_S0_Pf
    .private_segment_fixed_size: 0
    .sgpr_count:     108
    .sgpr_spill_count: 0
    .symbol:         _Z4k_t2PKfS0_S0_S0_S0_S0_PK15HIP_vector_typeIiLj4EEPKiPdPiS0_S0_Pf.kd
    .uniform_work_group_size: 1
    .uses_dynamic_stack: false
    .vgpr_count:     160
    .vgpr_spill_count: 0
    .wavefront_size: 64
